# grid barrier flat release: non-last workgroups spin on the global generation word instead of the per-XCD relay word (one relay hop less per barrier)
# speedup vs baseline: 1.0027x; 1.0018x over previous
; __device__ __forceinline__ unsigned xb_ld(unsigned* p)              { return __hip_atomic_load(p, __ATOMIC_RELAXED, __HIP_MEMORY_SCOPE_AGENT); }
; __device__ __forceinline__ unsigned xb_add(unsigned* p, unsigned v) { return __hip_atomic_fetch_add(p, v, __ATOMIC_RELAXED, __HIP_MEMORY_SCOPE_AGENT); }
; #define XB_SPIN(cond, bar) do { unsigned _sp = 0; while (cond) { __builtin_amdgcn_s_sleep(1); \
;     if ((++_sp & 255u) == 0u) { if (xb_ld(&(bar)[XB_TMO])) break; if (_sp > XB_SPIN_CAP) { atomicAdd(&(bar)[XB_TMO], 1u); break; } } } } while (0)
; __device__ __forceinline__ void xcd_barrier(const XcdBarrier& b) {
;     ...
;         const unsigned old = xb_add(&bar[XB_XSUB(b.x)], 1u);
;         const unsigned gen = old / nloc;
;         if (old + 1u == (gen + 1u) * nloc) {
;             __builtin_amdgcn_fence(__ATOMIC_RELEASE, "agent");
;             asm volatile("s_waitcnt vmcnt(0)" ::: "memory");
;             const unsigned og = xb_add(&bar[XB_TOP], 1u);
;             const unsigned tg = og / nx;
;             if (og + 1u == (tg + 1u) * nx) xb_add(&bar[XB_TOPGEN], 1u);
;             else XB_SPIN(xb_ld(&bar[XB_TOPGEN]) == tg, bar);
;             __builtin_amdgcn_fence(__ATOMIC_ACQUIRE, "agent");
;             xb_add(&bar[XB_XGEN(b.x)], 1u);
;             asm volatile("s_waitcnt vmcnt(0)" ::: "memory");
;         } else {
;             XB_SPIN(xb_ld(&bar[XB_XGEN(b.x)]) == gen, bar);
;             __builtin_amdgcn_fence(__ATOMIC_ACQUIRE, "agent");
;             asm volatile("s_waitcnt vmcnt(0)" ::: "memory");
;         }
.LBB0_40:
	s_or_b64 exec, exec, s[8:9]
	v_cvt_f32_u32_e32 v6, v4
	s_waitcnt vmcnt(0)
	v_readfirstlane_b32 s8, v5
	v_sub_u32_e32 v5, 0, v4
	v_rcp_iflag_f32_e32 v6, v6
	v_add_u32_e32 v7, s8, v3
	v_mul_f32_e32 v6, 0x4f7ffffe, v6
	v_cvt_u32_f32_e32 v6, v6
	v_mul_lo_u32 v3, v5, v6
	v_mul_hi_u32 v3, v6, v3
	v_add_u32_e32 v3, v6, v3
	v_mul_hi_u32 v3, v7, v3
	v_mul_lo_u32 v5, v3, v4
	v_sub_u32_e32 v5, v7, v5
	v_add_u32_e32 v6, 1, v3
	v_cmp_ge_u32_e32 vcc, v5, v4
	s_nop 1
	v_cndmask_b32_e32 v3, v3, v6, vcc
	v_sub_u32_e32 v6, v5, v4
	v_cndmask_b32_e32 v5, v5, v6, vcc
	v_add_u32_e32 v6, 1, v3
	v_cmp_ge_u32_e32 vcc, v5, v4
	v_add_u32_e32 v5, 1, v7
	s_nop 0
	v_cndmask_b32_e32 v3, v3, v6, vcc
	v_mul_lo_u32 v6, v4, v3
	v_add_u32_e32 v4, v6, v4
	v_cmp_ne_u32_e32 vcc, v5, v4
	s_and_saveexec_b64 s[8:9], vcc
	s_xor_b64 s[8:9], exec, s[8:9]
	s_cbranch_execz .LBB0_54
	v_readlane_b32 s10, v254, 21
	s_waitcnt lgkmcnt(0)
	v_mov_b32_e32 v2, 0
	v_readlane_b32 s11, v254, 22
	s_nop 4
	global_load_dword v4, v2, s[10:11] sc1
	s_waitcnt vmcnt(0)
	v_cmp_eq_u32_e32 vcc, v4, v3
	s_and_saveexec_b64 s[10:11], vcc
	s_cbranch_execz .LBB0_53
	s_mov_b32 s22, 1
	s_mov_b64 s[12:13], 0
	s_branch .LBB0_44

; __device__ __forceinline__ unsigned xb_ld(unsigned* p)              { return __hip_atomic_load(p, __ATOMIC_RELAXED, __HIP_MEMORY_SCOPE_AGENT); }
; #define XB_SPIN(cond, bar) do { unsigned _sp = 0; while (cond) { __builtin_amdgcn_s_sleep(1); \
;     if ((++_sp & 255u) == 0u) { if (xb_ld(&(bar)[XB_TMO])) break; if (_sp > XB_SPIN_CAP) { atomicAdd(&(bar)[XB_TMO], 1u); break; } } } } while (0)
; __device__ __forceinline__ void xcd_barrier(const XcdBarrier& b) {
;     ...
;             XB_SPIN(xb_ld(&bar[XB_XGEN(b.x)]) == gen, bar);
.LBB0_46:
	v_readlane_b32 s16, v254, 21
	v_readlane_b32 s17, v254, 22
	s_add_i32 s22, s22, 1
	s_mov_b64 s[18:19], -1
	s_nop 2
	global_load_dword v4, v2, s[16:17] sc1
	s_waitcnt vmcnt(0)
	v_cmp_ne_u32_e32 vcc, v4, v3
	s_orn2_b64 s[16:17], vcc, exec
	s_branch .LBB0_43

; __device__ __forceinline__ unsigned xb_ld(unsigned* p)              { return __hip_atomic_load(p, __ATOMIC_RELAXED, __HIP_MEMORY_SCOPE_AGENT); }
; __device__ __forceinline__ unsigned xb_add(unsigned* p, unsigned v) { return __hip_atomic_fetch_add(p, v, __ATOMIC_RELAXED, __HIP_MEMORY_SCOPE_AGENT); }
; #define XB_SPIN(cond, bar) do { unsigned _sp = 0; while (cond) { __builtin_amdgcn_s_sleep(1); \
;     if ((++_sp & 255u) == 0u) { if (xb_ld(&(bar)[XB_TMO])) break; if (_sp > XB_SPIN_CAP) { atomicAdd(&(bar)[XB_TMO], 1u); break; } } } } while (0)
; __device__ __forceinline__ void xcd_barrier(const XcdBarrier& b) {
;     ...
;         const unsigned old = xb_add(&bar[XB_XSUB(b.x)], 1u);
;         const unsigned gen = old / nloc;
;         if (old + 1u == (gen + 1u) * nloc) {
;             __builtin_amdgcn_fence(__ATOMIC_RELEASE, "agent");
;             asm volatile("s_waitcnt vmcnt(0)" ::: "memory");
;             const unsigned og = xb_add(&bar[XB_TOP], 1u);
;             const unsigned tg = og / nx;
;             if (og + 1u == (tg + 1u) * nx) xb_add(&bar[XB_TOPGEN], 1u);
;             else XB_SPIN(xb_ld(&bar[XB_TOPGEN]) == tg, bar);
;             __builtin_amdgcn_fence(__ATOMIC_ACQUIRE, "agent");
;             xb_add(&bar[XB_XGEN(b.x)], 1u);
;             asm volatile("s_waitcnt vmcnt(0)" ::: "memory");
;         } else {
;             XB_SPIN(xb_ld(&bar[XB_XGEN(b.x)]) == gen, bar);
;             __builtin_amdgcn_fence(__ATOMIC_ACQUIRE, "agent");
;             asm volatile("s_waitcnt vmcnt(0)" ::: "memory");
;         }
.LBB0_790:
	s_or_b64 exec, exec, s[6:7]
	v_cvt_f32_u32_e32 v6, v4
	s_waitcnt vmcnt(0)
	v_readfirstlane_b32 s3, v5
	v_sub_u32_e32 v5, 0, v4
	v_rcp_iflag_f32_e32 v6, v6
	v_add_u32_e32 v7, s3, v1
	v_mul_f32_e32 v6, 0x4f7ffffe, v6
	v_cvt_u32_f32_e32 v6, v6
	v_mul_lo_u32 v1, v5, v6
	v_mul_hi_u32 v1, v6, v1
	v_add_u32_e32 v1, v6, v1
	v_mul_hi_u32 v1, v7, v1
	v_mul_lo_u32 v5, v1, v4
	v_sub_u32_e32 v5, v7, v5
	v_add_u32_e32 v6, 1, v1
	v_cmp_ge_u32_e32 vcc, v5, v4
	s_nop 1
	v_cndmask_b32_e32 v1, v1, v6, vcc
	v_sub_u32_e32 v6, v5, v4
	v_cndmask_b32_e32 v5, v5, v6, vcc
	v_add_u32_e32 v6, 1, v1
	v_cmp_ge_u32_e32 vcc, v5, v4
	v_add_u32_e32 v5, 1, v7
	s_nop 0
	v_cndmask_b32_e32 v1, v1, v6, vcc
	v_mul_lo_u32 v6, v4, v1
	v_add_u32_e32 v4, v6, v4
	v_cmp_ne_u32_e32 vcc, v5, v4
	s_and_saveexec_b64 s[6:7], vcc
	s_xor_b64 s[6:7], exec, s[6:7]
	s_cbranch_execz .LBB0_804
	v_readlane_b32 s10, v254, 21
	v_readlane_b32 s11, v254, 22
	s_waitcnt lgkmcnt(0)
	s_nop 3
	global_load_dword v2, v3, s[10:11] sc1
	s_waitcnt vmcnt(0)
	v_cmp_eq_u32_e32 vcc, v2, v1
	s_and_saveexec_b64 s[10:11], vcc
	s_cbranch_execz .LBB0_803
	s_mov_b32 s3, 1
	s_mov_b64 s[12:13], 0
	s_branch .LBB0_794

; __device__ __forceinline__ unsigned xb_ld(unsigned* p)              { return __hip_atomic_load(p, __ATOMIC_RELAXED, __HIP_MEMORY_SCOPE_AGENT); }
; __device__ __forceinline__ unsigned xb_add(unsigned* p, unsigned v) { return __hip_atomic_fetch_add(p, v, __ATOMIC_RELAXED, __HIP_MEMORY_SCOPE_AGENT); }
; #define XB_SPIN(cond, bar) do { unsigned _sp = 0; while (cond) { __builtin_amdgcn_s_sleep(1); \
;     if ((++_sp & 255u) == 0u) { if (xb_ld(&(bar)[XB_TMO])) break; if (_sp > XB_SPIN_CAP) { atomicAdd(&(bar)[XB_TMO], 1u); break; } } } } while (0)
; __device__ __forceinline__ void xcd_barrier(const XcdBarrier& b) {
;     ...
;         const unsigned old = xb_add(&bar[XB_XSUB(b.x)], 1u);
;         const unsigned gen = old / nloc;
;         if (old + 1u == (gen + 1u) * nloc) {
;             __builtin_amdgcn_fence(__ATOMIC_RELEASE, "agent");
;             asm volatile("s_waitcnt vmcnt(0)" ::: "memory");
;             const unsigned og = xb_add(&bar[XB_TOP], 1u);
;             const unsigned tg = og / nx;
;             if (og + 1u == (tg + 1u) * nx) xb_add(&bar[XB_TOPGEN], 1u);
;             else XB_SPIN(xb_ld(&bar[XB_TOPGEN]) == tg, bar);
;             __builtin_amdgcn_fence(__ATOMIC_ACQUIRE, "agent");
;             xb_add(&bar[XB_XGEN(b.x)], 1u);
;             asm volatile("s_waitcnt vmcnt(0)" ::: "memory");
;         } else {
;             XB_SPIN(xb_ld(&bar[XB_XGEN(b.x)]) == gen, bar);
;             __builtin_amdgcn_fence(__ATOMIC_ACQUIRE, "agent");
;             asm volatile("s_waitcnt vmcnt(0)" ::: "memory");
;         }
.LBB0_1434:
	s_or_b64 exec, exec, s[4:5]
	v_cvt_f32_u32_e32 v6, v4
	s_waitcnt vmcnt(0)
	v_readfirstlane_b32 s2, v5
	v_sub_u32_e32 v5, 0, v4
	v_rcp_iflag_f32_e32 v6, v6
	v_add_u32_e32 v7, s2, v1
	v_mul_f32_e32 v6, 0x4f7ffffe, v6
	v_cvt_u32_f32_e32 v6, v6
	v_mul_lo_u32 v1, v5, v6
	v_mul_hi_u32 v1, v6, v1
	v_add_u32_e32 v1, v6, v1
	v_mul_hi_u32 v1, v7, v1
	v_mul_lo_u32 v5, v1, v4
	v_sub_u32_e32 v5, v7, v5
	v_add_u32_e32 v6, 1, v1
	v_cmp_ge_u32_e32 vcc, v5, v4
	s_nop 1
	v_cndmask_b32_e32 v1, v1, v6, vcc
	v_sub_u32_e32 v6, v5, v4
	v_cndmask_b32_e32 v5, v5, v6, vcc
	v_add_u32_e32 v6, 1, v1
	v_cmp_ge_u32_e32 vcc, v5, v4
	v_add_u32_e32 v5, 1, v7
	s_nop 0
	v_cndmask_b32_e32 v1, v1, v6, vcc
	v_mul_lo_u32 v6, v4, v1
	v_add_u32_e32 v4, v6, v4
	v_cmp_ne_u32_e32 vcc, v5, v4
	s_and_saveexec_b64 s[2:3], vcc
	s_xor_b64 s[4:5], exec, s[2:3]
	s_cbranch_execz .LBB0_1448
	v_readlane_b32 s2, v254, 21
	v_readlane_b32 s3, v254, 22
	s_waitcnt lgkmcnt(0)
	s_nop 3
	global_load_dword v2, v3, s[2:3] sc1
	s_waitcnt vmcnt(0)
	v_cmp_eq_u32_e32 vcc, v2, v1
	s_and_saveexec_b64 s[6:7], vcc
	s_cbranch_execz .LBB0_1447
	s_mov_b32 s2, 1
	s_mov_b64 s[12:13], 0
	s_branch .LBB0_1438

; __device__ __forceinline__ unsigned xb_ld(unsigned* p)              { return __hip_atomic_load(p, __ATOMIC_RELAXED, __HIP_MEMORY_SCOPE_AGENT); }
; __device__ __forceinline__ unsigned xb_add(unsigned* p, unsigned v) { return __hip_atomic_fetch_add(p, v, __ATOMIC_RELAXED, __HIP_MEMORY_SCOPE_AGENT); }
; #define XB_SPIN(cond, bar) do { unsigned _sp = 0; while (cond) { __builtin_amdgcn_s_sleep(1); \
;     if ((++_sp & 255u) == 0u) { if (xb_ld(&(bar)[XB_TMO])) break; if (_sp > XB_SPIN_CAP) { atomicAdd(&(bar)[XB_TMO], 1u); break; } } } } while (0)
; __device__ __forceinline__ void xcd_barrier(const XcdBarrier& b) {
;     ...
;         const unsigned old = xb_add(&bar[XB_XSUB(b.x)], 1u);
;         const unsigned gen = old / nloc;
;         if (old + 1u == (gen + 1u) * nloc) {
;             __builtin_amdgcn_fence(__ATOMIC_RELEASE, "agent");
;             asm volatile("s_waitcnt vmcnt(0)" ::: "memory");
;             const unsigned og = xb_add(&bar[XB_TOP], 1u);
;             const unsigned tg = og / nx;
;             if (og + 1u == (tg + 1u) * nx) xb_add(&bar[XB_TOPGEN], 1u);
;             else XB_SPIN(xb_ld(&bar[XB_TOPGEN]) == tg, bar);
;             __builtin_amdgcn_fence(__ATOMIC_ACQUIRE, "agent");
;             xb_add(&bar[XB_XGEN(b.x)], 1u);
;             asm volatile("s_waitcnt vmcnt(0)" ::: "memory");
;         } else {
;             XB_SPIN(xb_ld(&bar[XB_XGEN(b.x)]) == gen, bar);
;             __builtin_amdgcn_fence(__ATOMIC_ACQUIRE, "agent");
;             asm volatile("s_waitcnt vmcnt(0)" ::: "memory");
;         }
.LBB0_1518:
	s_or_b64 exec, exec, s[6:7]
	v_cvt_f32_u32_e32 v6, v4
	s_waitcnt vmcnt(0)
	v_readfirstlane_b32 s3, v5
	v_sub_u32_e32 v5, 0, v4
	v_rcp_iflag_f32_e32 v6, v6
	v_add_u32_e32 v7, s3, v1
	v_mul_f32_e32 v6, 0x4f7ffffe, v6
	v_cvt_u32_f32_e32 v6, v6
	v_mul_lo_u32 v1, v5, v6
	v_mul_hi_u32 v1, v6, v1
	v_add_u32_e32 v1, v6, v1
	v_mul_hi_u32 v1, v7, v1
	v_mul_lo_u32 v5, v1, v4
	v_sub_u32_e32 v5, v7, v5
	v_add_u32_e32 v6, 1, v1
	v_cmp_ge_u32_e32 vcc, v5, v4
	s_nop 1
	v_cndmask_b32_e32 v1, v1, v6, vcc
	v_sub_u32_e32 v6, v5, v4
	v_cndmask_b32_e32 v5, v5, v6, vcc
	v_add_u32_e32 v6, 1, v1
	v_cmp_ge_u32_e32 vcc, v5, v4
	v_add_u32_e32 v5, 1, v7
	s_nop 0
	v_cndmask_b32_e32 v1, v1, v6, vcc
	v_mul_lo_u32 v6, v4, v1
	v_add_u32_e32 v4, v6, v4
	v_cmp_ne_u32_e32 vcc, v5, v4
	s_and_saveexec_b64 s[6:7], vcc
	s_xor_b64 s[6:7], exec, s[6:7]
	s_cbranch_execz .LBB0_1532
	v_readlane_b32 s12, v254, 21
	v_readlane_b32 s13, v254, 22
	s_waitcnt lgkmcnt(0)
	s_nop 3
	global_load_dword v2, v3, s[12:13] sc1
	s_waitcnt vmcnt(0)
	v_cmp_eq_u32_e32 vcc, v2, v1
	s_and_saveexec_b64 s[12:13], vcc
	s_cbranch_execz .LBB0_1531
	s_mov_b32 s3, 1
	s_mov_b64 s[14:15], 0
	s_branch .LBB0_1522
